# E39: E37 + MoE-down epilogue issues the slot-index loads before the bias loads and waits only for them (counted vmcnt) before requesting gates
# speedup vs baseline: 1.0234x; 1.0006x over previous
.LBB0_1713:
	s_lshl_b32 s7, s30, 2
	s_add_i32 s7, s7, 0
	s_add_i32 s7, s7, 0x22700
	v_mov_b32_e32 v142, s7
	ds_read_b32 v142, v142
	s_lshl_b32 s7, s52, 2
	s_add_i32 s7, s7, 0
	s_add_i32 s7, s7, 0x22c00
	s_waitcnt lgkmcnt(0)
	v_readfirstlane_b32 s25, v142
	v_mov_b32_e32 v142, s7
	ds_read_b32 v142, v142
	v_add_u32_e32 v147, s25, v131
	s_waitcnt lgkmcnt(0)
	v_readfirstlane_b32 s7, v142
	s_nop 1
	v_cmp_gt_i32_e32 vcc, s7, v147
	v_lshl_or_b32 v142, s6, 8, v145
	v_cmp_gt_i32_e32 vcc, s7, v147
	s_and_saveexec_b64 s[30:31], vcc
	v_lshl_add_u32 v196, s52, 14, v147
	v_ashrrev_i32_e32 v197, 31, v196
	v_lshl_add_u64 v[196:197], v[196:197], 2, s[12:13]
	global_load_dword v180, v[196:197], off
	s_or_b64 exec, exec, s[30:31]
	v_add_u32_e32 v198, 16, v147
	v_cmp_gt_i32_e32 vcc, s7, v198
	s_and_saveexec_b64 s[30:31], vcc
	v_lshl_add_u32 v196, s52, 14, v198
	v_ashrrev_i32_e32 v197, 31, v196
	v_lshl_add_u64 v[196:197], v[196:197], 2, s[12:13]
	global_load_dword v181, v[196:197], off
	s_or_b64 exec, exec, s[30:31]
	v_add_u32_e32 v198, 32, v147
	v_cmp_gt_i32_e32 vcc, s7, v198
	s_and_saveexec_b64 s[30:31], vcc
	v_lshl_add_u32 v196, s52, 14, v198
	v_ashrrev_i32_e32 v197, 31, v196
	v_lshl_add_u64 v[196:197], v[196:197], 2, s[12:13]
	global_load_dword v182, v[196:197], off
	s_or_b64 exec, exec, s[30:31]
	v_add_u32_e32 v198, 48, v147
	v_cmp_gt_i32_e32 vcc, s7, v198
	s_and_saveexec_b64 s[30:31], vcc
	v_lshl_add_u32 v196, s52, 14, v198
	v_ashrrev_i32_e32 v197, 31, v196
	v_lshl_add_u64 v[196:197], v[196:197], 2, s[12:13]
	global_load_dword v183, v[196:197], off
	s_or_b64 exec, exec, s[30:31]
	v_add_u32_e32 v198, 128, v147
	v_cmp_gt_i32_e32 vcc, s7, v198
	s_and_saveexec_b64 s[30:31], vcc
	v_lshl_add_u32 v196, s52, 14, v198
	v_ashrrev_i32_e32 v197, 31, v196
	v_lshl_add_u64 v[196:197], v[196:197], 2, s[12:13]
	global_load_dword v184, v[196:197], off
	s_or_b64 exec, exec, s[30:31]
	v_add_u32_e32 v198, 144, v147
	v_cmp_gt_i32_e32 vcc, s7, v198
	s_and_saveexec_b64 s[30:31], vcc
	v_lshl_add_u32 v196, s52, 14, v198
	v_ashrrev_i32_e32 v197, 31, v196
	v_lshl_add_u64 v[196:197], v[196:197], 2, s[12:13]
	global_load_dword v185, v[196:197], off
	s_or_b64 exec, exec, s[30:31]
	v_add_u32_e32 v198, 160, v147
	v_cmp_gt_i32_e32 vcc, s7, v198
	s_and_saveexec_b64 s[30:31], vcc
	v_lshl_add_u32 v196, s52, 14, v198
	v_ashrrev_i32_e32 v197, 31, v196
	v_lshl_add_u64 v[196:197], v[196:197], 2, s[12:13]
	global_load_dword v186, v[196:197], off
	s_or_b64 exec, exec, s[30:31]
	v_add_u32_e32 v198, 176, v147
	v_cmp_gt_i32_e32 vcc, s7, v198
	s_and_saveexec_b64 s[30:31], vcc
	v_lshl_add_u32 v196, s52, 14, v198
	v_ashrrev_i32_e32 v197, 31, v196
	v_lshl_add_u64 v[196:197], v[196:197], 2, s[12:13]
	global_load_dword v187, v[196:197], off
	s_or_b64 exec, exec, s[30:31]
	s_add_i32 s34, s52, s50
	s_ashr_i32 s35, s34, 31
	s_lshl_b64 s[34:35], s[34:35], 12
	s_add_u32 s34, s44, s34
	v_ashrrev_i32_e32 v143, 31, v142
	s_addc_u32 s35, s16, s35
	v_lshl_add_u64 v[162:163], v[142:143], 2, s[34:35]
	global_load_dwordx4 v[164:167], v[162:163], off
	global_load_dwordx4 v[168:171], v[162:163], off offset:16
	global_load_dwordx4 v[172:175], v[162:163], off offset:512
	global_load_dwordx4 v[176:179], v[162:163], off offset:528
	s_waitcnt vmcnt(4)
	v_cmp_gt_i32_e32 vcc, s7, v147
	s_and_saveexec_b64 s[30:31], vcc
	v_mov_b32_e32 v196, v180
	v_ashrrev_i32_e32 v197, 31, v196
	v_lshl_add_u64 v[196:197], v[196:197], 2, s[14:15]
	global_load_dword v188, v[196:197], off
	s_or_b64 exec, exec, s[30:31]
	v_add_u32_e32 v198, 16, v147
	v_cmp_gt_i32_e32 vcc, s7, v198
	s_and_saveexec_b64 s[30:31], vcc
	v_mov_b32_e32 v196, v181
	v_ashrrev_i32_e32 v197, 31, v196
	v_lshl_add_u64 v[196:197], v[196:197], 2, s[14:15]
	global_load_dword v189, v[196:197], off
	s_or_b64 exec, exec, s[30:31]
	v_add_u32_e32 v198, 32, v147
	v_cmp_gt_i32_e32 vcc, s7, v198
	s_and_saveexec_b64 s[30:31], vcc
	v_mov_b32_e32 v196, v182
	v_ashrrev_i32_e32 v197, 31, v196
	v_lshl_add_u64 v[196:197], v[196:197], 2, s[14:15]
	global_load_dword v190, v[196:197], off
	s_or_b64 exec, exec, s[30:31]
	v_add_u32_e32 v198, 48, v147
	v_cmp_gt_i32_e32 vcc, s7, v198
	s_and_saveexec_b64 s[30:31], vcc
	v_mov_b32_e32 v196, v183
	v_ashrrev_i32_e32 v197, 31, v196
	v_lshl_add_u64 v[196:197], v[196:197], 2, s[14:15]
	global_load_dword v191, v[196:197], off
	s_or_b64 exec, exec, s[30:31]
	v_add_u32_e32 v198, 128, v147
	v_cmp_gt_i32_e32 vcc, s7, v198
	s_and_saveexec_b64 s[30:31], vcc
	v_mov_b32_e32 v196, v184
	v_ashrrev_i32_e32 v197, 31, v196
	v_lshl_add_u64 v[196:197], v[196:197], 2, s[14:15]
	global_load_dword v192, v[196:197], off
	s_or_b64 exec, exec, s[30:31]
	v_add_u32_e32 v198, 144, v147
	v_cmp_gt_i32_e32 vcc, s7, v198
	s_and_saveexec_b64 s[30:31], vcc
	v_mov_b32_e32 v196, v185
	v_ashrrev_i32_e32 v197, 31, v196
	v_lshl_add_u64 v[196:197], v[196:197], 2, s[14:15]
	global_load_dword v193, v[196:197], off
	s_or_b64 exec, exec, s[30:31]
	v_add_u32_e32 v198, 160, v147
	v_cmp_gt_i32_e32 vcc, s7, v198
	s_and_saveexec_b64 s[30:31], vcc
	v_mov_b32_e32 v196, v186
	v_ashrrev_i32_e32 v197, 31, v196
	v_lshl_add_u64 v[196:197], v[196:197], 2, s[14:15]
	global_load_dword v194, v[196:197], off
	s_or_b64 exec, exec, s[30:31]
	v_add_u32_e32 v198, 176, v147
	v_cmp_gt_i32_e32 vcc, s7, v198
	s_and_saveexec_b64 s[30:31], vcc
	v_mov_b32_e32 v196, v187
	v_ashrrev_i32_e32 v197, 31, v196
	v_lshl_add_u64 v[196:197], v[196:197], 2, s[14:15]
	global_load_dword v195, v[196:197], off
	s_or_b64 exec, exec, s[30:31]
	s_waitcnt vmcnt(0)
	v_cmp_gt_i32_e32 vcc, s7, v147
	s_and_saveexec_b64 s[30:31], vcc
	s_cbranch_execz .LBB0_1715
	v_lshl_add_u32 v148, s52, 14, v147
	v_ashrrev_i32_e32 v149, 31, v148
	v_lshl_add_u64 v[148:149], v[148:149], 2, s[12:13]
	v_mov_b32_e32 v156, v180
	s_add_i32 s34, s52, s50
	s_ashr_i32 s35, s34, 31
	s_lshl_b64 s[34:35], s[34:35], 12
	s_add_u32 s34, s44, s34
	v_ashrrev_i32_e32 v143, 31, v142
	s_addc_u32 s35, s16, s35
	v_lshl_add_u64 v[158:159], v[142:143], 2, s[34:35]
	v_ashrrev_i32_e32 v157, 31, v156
	v_lshl_add_u64 v[160:161], v[156:157], 2, s[14:15]
	v_mov_b32_e32 v160, v188
	v_lshlrev_b64 v[156:157], 11, v[156:157]
	v_lshl_add_u64 v[156:157], s[10:11], 0, v[156:157]
	v_pk_add_f32 v[128:129], v[128:129], v[166:167]
	v_pk_add_f32 v[124:125], v[124:125], v[170:171]
	v_pk_add_f32 v[122:123], v[122:123], v[168:169]
	v_pk_add_f32 v[126:127], v[126:127], v[164:165]
	v_lshl_add_u64 v[148:149], v[142:143], 1, v[156:157]
	v_pk_mul_f32 v[150:151], v[160:161], v[124:125] op_sel_hi:[0,1]
	v_pk_mul_f32 v[124:125], v[160:161], v[122:123] op_sel_hi:[0,1]
	v_pk_mul_f32 v[128:129], v[160:161], v[128:129] op_sel_hi:[0,1]
	v_pk_mul_f32 v[126:127], v[160:161], v[126:127] op_sel_hi:[0,1]
	v_cvt_pk_bf16_f32 v122, v126, v127
	v_cvt_pk_bf16_f32 v123, v128, v129
	v_cvt_pk_bf16_f32 v124, v124, v125
	v_cvt_pk_bf16_f32 v125, v150, v151
	global_store_dwordx4 v[148:149], v[122:125], off
	v_pk_add_f32 v[120:121], v[120:121], v[174:175]
	v_pk_add_f32 v[116:117], v[116:117], v[178:179]
	v_pk_add_f32 v[114:115], v[114:115], v[176:177]
	v_pk_add_f32 v[118:119], v[118:119], v[172:173]
	v_pk_mul_f32 v[122:123], v[160:161], v[116:117] op_sel_hi:[0,1]
	v_pk_mul_f32 v[116:117], v[160:161], v[114:115] op_sel_hi:[0,1]
	v_pk_mul_f32 v[120:121], v[160:161], v[120:121] op_sel_hi:[0,1]
	v_pk_mul_f32 v[118:119], v[160:161], v[118:119] op_sel_hi:[0,1]
	v_cvt_pk_bf16_f32 v114, v118, v119
	v_cvt_pk_bf16_f32 v115, v120, v121
	v_cvt_pk_bf16_f32 v116, v116, v117
	v_cvt_pk_bf16_f32 v117, v122, v123
	global_store_dwordx4 v[148:149], v[114:117], off offset:256
